# edge_main prologue: scalar loads hoisted, idx0 wait moved to first consumer
# speedup vs baseline: 1.0065x; 1.0065x over previous
_Z9edge_mainPKfS0_PKiS2_PKcPcS0_S0_Pf:
	s_load_dwordx8 s[8:15], s[0:1], 0x0
	s_load_dwordx4 s[16:19], s[0:1], 0x20
	s_load_dwordx4 s[20:23], s[0:1], 0x30
	s_load_dwordx2 s[24:25], s[0:1], 0x40
	v_and_b32_e32 v2, 16, v0
	v_lshrrev_b32_e32 v1, 6, v0
	v_cmp_eq_u32_e32 vcc, 0, v2
	v_and_b32_e32 v106, 15, v0
	s_waitcnt lgkmcnt(0)
	v_mov_b32_e32 v3, s15
	v_mov_b32_e32 v4, s13
	v_cndmask_b32_e32 v95, v3, v4, vcc
	v_mov_b32_e32 v2, s14
	v_mov_b32_e32 v3, s12
	v_lshl_add_u32 v62, v1, 8, s2
	v_cndmask_b32_e32 v94, v2, v3, vcc
	v_lshl_or_b32 v2, v62, 4, v106
	v_ashrrev_i32_e32 v3, 31, v2
	v_lshl_add_u64 v[4:5], v[2:3], 2, v[94:95]
	v_add_u32_e32 v2, 0x8000, v2
	v_ashrrev_i32_e32 v3, 31, v2
	v_lshl_add_u64 v[2:3], v[2:3], 2, v[94:95]
	global_load_dword v60, v[4:5], off
	global_load_dword v64, v[2:3], off
	v_and_b32_e32 v70, 63, v0
	v_lshlrev_b32_e32 v68, 4, v70
	v_mov_b32_e32 v69, 0
	v_mov_b32_e32 v2, 0x30d40
	v_bfe_u32 v65, v0, 3, 3
	v_and_b32_e32 v66, 0x70, v68
	v_cndmask_b32_e64 v2, v2, 0, vcc
	v_mov_b32_e32 v3, v69
	v_mov_b32_e32 v67, v69
	v_lshlrev_b32_e32 v58, 4, v0
	v_mov_b32_e32 v59, v69
	s_waitcnt lgkmcnt(0)
	v_lshl_add_u64 v[4:5], s[16:17], 0, v[58:59]
	s_movk_i32 s3, 0x2000
	v_add_co_u32_e32 v6, vcc, s3, v4
	s_movk_i32 s3, 0x6000
	s_nop 0
	v_addc_co_u32_e32 v7, vcc, 0, v5, vcc
	global_load_dwordx4 v[72:75], v58, s[16:17]
	v_or_b32_e32 v8, 0x4000, v58
	global_load_dwordx4 v[76:79], v[6:7], off
	global_load_dwordx4 v[80:83], v8, s[16:17]
	v_add_co_u32_e32 v6, vcc, s3, v4
	s_mov_b32 s3, 0xa000
	s_nop 0
	v_addc_co_u32_e32 v7, vcc, 0, v5, vcc
	v_or_b32_e32 v8, 0x8000, v58
	global_load_dwordx4 v[84:87], v[6:7], off
	global_load_dwordx4 v[88:91], v8, s[16:17]
	v_add_co_u32_e32 v6, vcc, s3, v4
	s_mov_b32 s3, 0xe000
	s_nop 0
	v_addc_co_u32_e32 v7, vcc, 0, v5, vcc
	v_lshl_add_u64 v[2:3], s[16:17], 0, v[2:3]
	s_mov_b64 s[4:5], 0x100000
	v_ashrrev_i32_e32 v63, 31, v62
	v_add_co_u32_e32 v4, vcc, s3, v4
	v_lshl_add_u64 v[96:97], v[2:3], 0, s[4:5]
	v_lshlrev_b64 v[2:3], 13, v[62:63]
	v_addc_co_u32_e32 v5, vcc, 0, v5, vcc
	v_lshl_add_u64 v[2:3], s[8:9], 0, v[2:3]
	v_or_b32_e32 v8, 0xc000, v58
	global_load_dwordx4 v[102:105], v[6:7], off
	global_load_dwordx4 v[110:113], v8, s[16:17]
	s_movk_i32 s3, 0x1000
	v_or_b32_e32 v6, 0x1200, v0
	v_cmp_gt_u32_e32 vcc, 32, v0
	v_lshl_add_u64 v[18:19], v[2:3], 0, v[68:69]
	v_add_co_u32_e64 v34, s[4:5], s3, v18
	v_cndmask_b32_e32 v6, 0, v6, vcc
	v_lshlrev_b32_e32 v6, 4, v6
	v_addc_co_u32_e64 v35, s[4:5], 0, v19, s[4:5]
	v_mbcnt_lo_u32_b32 v36, -1, 0
	global_load_dwordx4 v[114:117], v[4:5], off
	global_load_dwordx4 v[54:57], v6, s[16:17]
	s_nop 0
	global_load_dwordx4 v[2:5], v[18:19], off nt
	global_load_dwordx4 v[6:9], v[18:19], off offset:1024 nt
	global_load_dwordx4 v[10:13], v[18:19], off offset:2048 nt
	global_load_dwordx4 v[14:17], v[18:19], off offset:3072 nt
	s_nop 0
	global_load_dwordx4 v[18:21], v[34:35], off nt
	global_load_dwordx4 v[22:25], v[34:35], off offset:1024 nt
	global_load_dwordx4 v[26:29], v[34:35], off offset:2048 nt
	global_load_dwordx4 v[30:33], v[34:35], off offset:3072 nt
	v_lshlrev_b64 v[34:35], 10, v[62:63]
	v_mbcnt_hi_u32_b32 v63, -1, v36
	v_and_or_b32 v36, v63, 64, v65
	v_lshlrev_b32_e32 v107, 2, v36
	s_waitcnt vmcnt(18)
	v_ashrrev_i32_e32 v61, 31, v60
	ds_bpermute_b32 v38, v107, v60
	ds_bpermute_b32 v40, v107, v60 offset:32
	v_lshl_add_u64 v[46:47], s[16:17], 0, v[66:67]
	s_mov_b64 s[4:5], 0x200000
	v_lshl_add_u64 v[98:99], v[46:47], 0, s[4:5]
	v_lshl_add_u64 v[34:35], s[10:11], 0, v[34:35]
	s_waitcnt lgkmcnt(1)
	v_lshlrev_b32_e32 v38, 7, v38
	v_mov_b32_e32 v39, v69
	v_lshl_add_u64 v[34:35], v[34:35], 0, v[68:69]
	v_lshl_add_u64 v[48:49], v[98:99], 0, v[38:39]
	s_waitcnt lgkmcnt(0)
	v_lshlrev_b32_e32 v38, 7, v40
	global_load_dwordx4 v[34:37], v[34:35], off nt
	v_lshl_add_u64 v[50:51], v[98:99], 0, v[38:39]
	global_load_dwordx4 v[38:41], v[48:49], off
	global_load_dwordx4 v[42:45], v[50:51], off
	ds_bpermute_b32 v48, v107, v60 offset:64
	ds_bpermute_b32 v49, v107, v60 offset:96
	s_mov_b64 s[4:5], 0x81a800
	v_lshl_add_u64 v[100:101], v[46:47], 0, s[4:5]
	v_mov_b32_e32 v47, v69
	s_waitcnt lgkmcnt(1)
	v_lshlrev_b32_e32 v46, 7, v48
	v_lshl_add_u64 v[92:93], v[100:101], 0, v[46:47]
	s_waitcnt lgkmcnt(0)
	v_lshlrev_b32_e32 v46, 7, v49
	v_lshl_add_u64 v[108:109], v[100:101], 0, v[46:47]
	v_lshl_add_u64 v[60:61], v[60:61], 2, v[96:97]
	global_load_dwordx4 v[46:49], v[92:93], off
	global_load_dwordx4 v[50:53], v[108:109], off
	v_or_b32_e32 v59, 0x1000, v0
	global_load_dword v108, v[60:61], off
	v_lshl_or_b32 v60, s2, 3, v1
	v_mov_b32_e32 v61, v69
	v_lshlrev_b64 v[60:61], 11, v[60:61]
	s_movk_i32 s3, 0x1220
	v_lshl_add_u64 v[60:61], s[18:19], 0, v[60:61]
	v_lshlrev_b32_e32 v92, 2, v70
	v_mov_b32_e32 v93, v69
	v_cmp_gt_u32_e64 s[4:5], s3, v59
	v_lshl_add_u64 v[60:61], v[60:61], 0, v[92:93]
	s_mov_b64 s[6:7], 0x2000000
	s_brev_b32 s3, 64
	v_lshl_add_u64 v[92:93], v[60:61], 0, s[6:7]
	v_add_co_u32_e64 v60, s[6:7], s3, v60
	s_nop 1
	v_addc_co_u32_e64 v61, s[6:7], 0, v61, s[6:7]
	global_store_dword v[60:61], v69, off
	global_store_dword v[92:93], v69, off offset:256
	global_store_dword v[92:93], v69, off offset:512
	global_store_dword v[92:93], v69, off offset:768
	global_store_dword v[92:93], v69, off offset:1024
	global_store_dword v[92:93], v69, off offset:1280
	global_store_dword v[92:93], v69, off offset:1536
	global_store_dword v[92:93], v69, off offset:1792
	s_waitcnt vmcnt(30)
	ds_write_b128 v58, v[72:75]
	s_waitcnt vmcnt(29)
	ds_write_b128 v58, v[76:79] offset:8192
	s_waitcnt vmcnt(28)
	ds_write_b128 v58, v[80:83] offset:16384
	s_waitcnt vmcnt(27)
	ds_write_b128 v58, v[84:87] offset:24576
	s_waitcnt vmcnt(26)
	ds_write_b128 v58, v[88:91] offset:32768
	s_waitcnt vmcnt(25)
	ds_write_b128 v58, v[102:105] offset:40960
	s_waitcnt vmcnt(24)
	ds_write_b128 v58, v[110:113] offset:49152
	s_waitcnt vmcnt(23)
	ds_write_b128 v58, v[114:117] offset:57344
	s_and_saveexec_b64 s[6:7], s[4:5]
	s_cbranch_execz .LBB1_2
	v_cndmask_b32_e64 v60, 0, v59, s[4:5]
	v_mov_b32_e32 v61, v69
	v_lshl_add_u64 v[60:61], v[60:61], 4, s[16:17]
	global_load_dwordx4 v[72:75], v[60:61], off
	v_lshlrev_b32_e32 v59, 4, v59
	s_waitcnt vmcnt(0)
	ds_write_b128 v59, v[72:75]

.LBB1_4:
	s_or_b64 exec, exec, s[4:5]
	s_mov_b32 s3, 0x927c
	v_cmp_gt_i32_e32 vcc, s3, v62
	s_waitcnt lgkmcnt(0)
	s_barrier
	s_and_saveexec_b64 s[4:5], vcc
	s_cbranch_execz .LBB1_7
	v_and_b32_e32 v67, 0x1f0, v58
	v_and_b32_e32 v76, 64, v63
	v_or_b32_e32 v77, v76, v106
	v_lshlrev_b32_e32 v114, 2, v77
	s_waitcnt lgkmcnt(0)
	global_load_dwordx4 v[54:57], v67, s[20:21]
	global_load_dwordx4 v[58:61], v67, s[22:23]
	v_xor_b32_e32 v77, 16, v63
	v_add_u32_e32 v76, 64, v76
	v_cmp_lt_i32_e32 vcc, v77, v76
	v_lshl_add_u64 v[102:103], s[8:9], 0, v[68:69]
	v_lshl_add_u64 v[104:105], s[10:11], 0, v[68:69]
	s_movk_i32 s1, 0x2800
	v_mov_b32_e32 v67, 0x12200
	v_and_b32_e32 v69, 48, v0
	v_lshrrev_b32_e32 v0, 1, v0
	v_cndmask_b32_e32 v77, v63, v77, vcc
	s_movk_i32 s0, 0x60
	v_mad_u32_u24 v67, v1, s1, v67
	s_movk_i32 s1, 0x120
	v_lshrrev_b32_e32 v73, 5, v70
	v_lshrrev_b32_e32 v70, 2, v70
	v_and_b32_e32 v0, 24, v0
	v_lshlrev_b32_e32 v116, 2, v77
	v_xor_b32_e32 v77, 32, v63
	v_mad_u32_u24 v112, v106, s1, v69
	s_movk_i32 s3, 0x220
	v_mad_u32_u24 v72, v106, s0, v67
	v_mad_u32_u24 v70, v70, s0, v67
	v_sub_u32_e32 v0, 0, v0
	v_cmp_lt_i32_e32 vcc, v77, v76
	s_lshl_b32 s0, s2, 13
	v_mad_u32_u24 v71, v106, s3, v67
	v_mad_u32_u24 v73, v73, s3, v67
	v_and_b32_e32 v74, 0x1f0, v68
	v_and_b32_e32 v75, 48, v68
	v_mad_u32_u24 v65, v65, s1, v67
	v_mad_u32_u24 v67, v106, s1, v67
	v_cndmask_b32_e32 v63, v63, v77, vcc
	v_lshl_add_u32 v1, v1, 21, s0
	s_movk_i32 s0, 0x1c00
	v_add_u32_e32 v0, v112, v0
	v_or_b32_e32 v109, 32, v107
	v_or_b32_e32 v110, 64, v107
	v_or_b32_e32 v111, 0x60, v107
	s_mov_b32 s7, 0x27000
	s_brev_b32 s6, -2
	s_mov_b32 s4, s24
	s_and_b32 s5, s25, 0xffff
	v_add_u32_e32 v113, 0x9000, v112
	v_or_b32_e32 v115, 64, v114
	v_lshlrev_b32_e32 v117, 2, v63
	v_or3_b32 v118, v1, v68, s0
	s_mov_b64 s[0:1], 0
	s_movk_i32 s3, 0x1000
	s_mov_b32 s8, 0x927b
	v_add_u32_e32 v119, v65, v66
	v_mov_b32_e32 v1, 0
	v_add_u32_e32 v120, v67, v69
	v_add_u32_e32 v121, v73, v74
	v_add_u32_e32 v122, v70, v75
	v_add_u32_e32 v123, v71, v69
	v_add_u32_e32 v124, v72, v69
	v_or_b32_e32 v125, 0x12000, v69
	v_or_b32_e32 v126, 0x12040, v69
	v_or_b32_e32 v127, 0x12080, v69
	v_or_b32_e32 v128, 0x120c0, v69
	v_or_b32_e32 v129, 0x12100, v69
	v_or_b32_e32 v130, 0x12140, v69
	v_or_b32_e32 v131, 0x12180, v69
	v_or_b32_e32 v132, 0x121c0, v69
	s_mov_b32 s2, 0xbf317218
	v_mov_b32_e32 v133, 0x3727c5ac
	v_add_u32_e32 v134, 0x100, v0
